# speedup vs baseline: 1.0043x; 1.0043x over previous
_Z13lstm_ta_fusedPKfPKDv8_DF16_S0_S0_S3_S0_PfP15HIP_vector_typeIjLj2EE:
	s_load_dwordx8 s[12:19], s[0:1], 0x0
	s_load_dwordx8 s[4:11], s[0:1], 0x20
	v_readfirstlane_b32 s35, v0
	s_lshr_b32 s28, s35, 6
	s_mul_i32 s40, s28, 0x6000
	s_mul_hi_u32 s3, s28, 0x6000
	s_waitcnt lgkmcnt(0)
	s_add_u32 s14, s14, s40
	v_bfe_u32 v1, v0, 2, 4
	s_addc_u32 s15, s15, s3
	s_lshl_b32 s33, s28, 4
	v_and_b32_e32 v204, 12, v1
	v_or_b32_e32 v2, s33, v204
	v_lshlrev_b32_e32 v2, 2, v2
	global_load_dwordx4 v[100:103], v2, s[16:17]
	global_load_dwordx4 v[108:111], v2, s[16:17] offset:512
	global_load_dwordx4 v[96:99], v2, s[18:19]
	global_load_dwordx4 v[130:133], v2, s[18:19] offset:512
	global_load_dwordx4 v[134:137], v2, s[16:17] offset:1024
	global_load_dwordx4 v[146:149], v2, s[16:17] offset:1536
	global_load_dwordx4 v[150:153], v2, s[18:19] offset:1024
	global_load_dwordx4 v[154:157], v2, s[18:19] offset:1536
	v_and_b32_e32 v170, 63, v0
	v_mov_b32_e32 v187, 0
	v_lshlrev_b32_e32 v186, 4, v170
	s_movk_i32 s3, 0x1000
	v_lshl_add_u64 v[22:23], s[14:15], 0, v[186:187]
	v_add_co_u32_e32 v24, vcc, s3, v22
	s_movk_i32 s17, 0x2000
	s_nop 0
	v_addc_co_u32_e32 v25, vcc, 0, v23, vcc
	v_add_co_u32_e32 v26, vcc, s17, v22
	s_lshl_b32 s34, s2, 4
	s_and_b32 s21, s13, 0xffff
	s_waitcnt lgkmcnt(0)
	s_and_b32 s17, s5, 0xffff
	s_mul_hi_u32 s0, s2, 0x32000
	s_mul_i32 s2, s2, 0x32000
	s_movk_i32 s36, 0x3000
	v_addc_co_u32_e32 v27, vcc, 0, v23, vcc
	s_add_u32 s2, s10, s2
	v_add_co_u32_e32 v30, vcc, s36, v22
	s_addc_u32 s3, s11, s0
	s_ashr_i32 s0, s34, 31
	s_movk_i32 s16, 0x4000
	v_addc_co_u32_e32 v31, vcc, 0, v23, vcc
	v_or_b32_e32 v164, s34, v1
	v_mov_b32_e32 v165, s0
	s_mov_b32 s29, 0
	v_add_co_u32_e32 v28, vcc, s16, v22
	v_lshlrev_b32_e32 v1, 1, v0
	s_movk_i32 s18, 0x5000
	v_addc_co_u32_e32 v29, vcc, 0, v23, vcc
	s_lshl_b32 s0, s28, 5
	s_mov_b32 s1, s29
	v_add_co_u32_e32 v94, vcc, s18, v22
	global_load_dwordx4 v[54:57], v186, s[14:15]
	global_load_dwordx4 v[58:61], v186, s[14:15] offset:1024
	global_load_dwordx4 v[62:65], v186, s[14:15] offset:2048
	global_load_dwordx4 v[50:53], v186, s[14:15] offset:3072
	v_addc_co_u32_e32 v95, vcc, 0, v23, vcc
	global_load_dwordx4 v[66:69], v[24:25], off offset:1024
	global_load_dwordx4 v[34:37], v[24:25], off offset:2048
	global_load_dwordx4 v[38:41], v[24:25], off offset:3072
	global_load_dwordx4 v[70:73], v[26:27], off offset:-4096
	global_load_dwordx4 v[42:45], v[26:27], off
	global_load_dwordx4 v[46:49], v[26:27], off offset:1024
	global_load_dwordx4 v[74:77], v[26:27], off offset:2048
	global_load_dwordx4 v[78:81], v[26:27], off offset:3072
	global_load_dwordx4 v[18:21], v[28:29], off offset:-4096
	global_load_dwordx4 v[14:17], v[30:31], off offset:1024
	global_load_dwordx4 v[10:13], v[30:31], off offset:2048
	global_load_dwordx4 v[82:85], v[28:29], off
	global_load_dwordx4 v[86:89], v[28:29], off offset:1024
	global_load_dwordx4 v[2:5], v[28:29], off offset:2048
	global_load_dwordx4 v[6:9], v[28:29], off offset:3072
	s_and_b32 s25, s3, 0xffff
	v_lshlrev_b32_e32 v188, 3, v0
	s_mov_b32 s10, 0xc038aa3b
	v_and_b32_e32 v205, 15, v0
	s_mov_b32 s11, 0xbfb8aa3b
	s_mov_b32 s23, 0x20000
	v_lshl_or_b32 v189, s28, 11, v186
	s_mov_b32 s22, 0x3200000
	s_mov_b32 s20, s12
	s_mov_b32 s18, 0xc8000
	s_mov_b32 s19, s23
	s_mov_b32 s26, 0x32000
	s_mov_b32 s24, s2
	s_mov_b32 s27, s23
	v_or_b32_e32 v208, 0x400, v189
	s_mov_b32 s37, 0x18000
	s_mov_b32 s38, 0xf149f2ca
	v_mov_b32_e32 v202, 0x42a00000
	v_mov_b32_e32 v200, v187
	v_mov_b32_e32 v201, v187
	v_mov_b32_e32 v198, v187
	v_mov_b32_e32 v199, v187
	s_waitcnt vmcnt(26)
	v_mov_b32_e32 v104, v100
	s_waitcnt vmcnt(25)
	v_mov_b32_e32 v105, v108
	v_mov_b32_e32 v108, v101
	v_lshlrev_b64 v[100:101], 8, v[164:165]
	s_waitcnt vmcnt(22)
	v_mov_b32_e32 v160, v136
	v_lshl_add_u64 v[100:101], s[12:13], 0, v[100:101]
	v_and_b32_e32 v136, 6, v1
	v_mov_b32_e32 v112, v134
	s_waitcnt vmcnt(21)
	v_mov_b32_e32 v113, v146
	v_mov_b32_e32 v146, v135
	v_mov_b32_e32 v134, v102
	v_mov_b32_e32 v135, v110
	v_mov_b32_e32 v110, v103
	v_lshl_add_u64 v[100:101], v[100:101], 0, s[0:1]
	v_lshlrev_b32_e32 v102, 2, v136
	v_mov_b32_e32 v103, v187
	v_lshl_add_u64 v[100:101], v[100:101], 0, v[102:103]
	s_mov_b32 s0, 0x100000
	v_add_co_u32_e32 v102, vcc, s0, v100
	s_mov_b32 s0, 0x200000
	s_nop 0
	v_addc_co_u32_e32 v103, vcc, 0, v101, vcc
	v_mov_b32_e32 v106, v96
	v_mov_b32_e32 v107, v130
	v_mov_b32_e32 v130, v97
	global_load_dwordx4 v[26:29], v[30:31], off offset:3072
	global_load_dwordx4 v[22:25], v[94:95], off
	s_nop 0
	global_load_dwordx4 v[30:33], v[94:95], off offset:1024
	global_load_dwordx4 v[90:93], v[94:95], off offset:2048
	s_nop 0
	global_load_dwordx4 v[94:97], v[94:95], off offset:3072
	s_nop 0
	global_load_dwordx2 v[166:167], v[100:101], off
	global_load_dwordx2 v[168:169], v[102:103], off
	v_add_co_u32_e32 v102, vcc, s0, v100
	s_mov_b32 s0, 0x300000
	s_nop 0
	v_addc_co_u32_e32 v103, vcc, 0, v101, vcc
	v_add_co_u32_e32 v114, vcc, s0, v100
	s_mov_b32 s0, 0x400000
	s_nop 0
	v_addc_co_u32_e32 v115, vcc, 0, v101, vcc
	global_load_dwordx2 v[196:197], v[102:103], off
	global_load_dwordx2 v[194:195], v[114:115], off
	v_add_co_u32_e32 v102, vcc, s0, v100
	s_mov_b32 s0, 0x500000
	s_nop 0
	v_addc_co_u32_e32 v103, vcc, 0, v101, vcc
	v_add_co_u32_e32 v100, vcc, s0, v100
	s_lshl_b64 s[0:1], s[28:29], 11
	s_add_u32 s0, s4, s0
	v_addc_co_u32_e32 v101, vcc, 0, v101, vcc
	s_addc_u32 s1, s5, s1
	global_load_dwordx2 v[192:193], v[102:103], off
	global_load_dwordx2 v[190:191], v[100:101], off
	v_lshl_add_u64 v[100:101], s[0:1], 0, v[186:187]
	v_add_co_u32_e32 v102, vcc, s16, v100
	global_load_dwordx4 v[138:141], v186, s[0:1]
	global_load_dwordx4 v[142:145], v186, s[0:1] offset:1024
	v_addc_co_u32_e32 v103, vcc, 0, v101, vcc
	s_mov_b32 s0, 0x8000
	v_add_co_u32_e32 v100, vcc, s0, v100
	global_load_dwordx4 v[122:125], v[102:103], off
	global_load_dwordx4 v[126:129], v[102:103], off offset:1024
	v_addc_co_u32_e32 v101, vcc, 0, v101, vcc
	global_load_dwordx4 v[114:117], v[100:101], off
	global_load_dwordx4 v[118:121], v[100:101], off offset:1024
	v_pk_add_f32 v[102:103], v[108:109], v[130:131]
	v_lshlrev_b32_e32 v130, 6, v164
	v_lshl_add_u32 v130, s28, 3, v130
	v_lshlrev_b32_e32 v1, 2, v170
	v_or_b32_e32 v130, v130, v136
	v_lshl_or_b32 v1, s28, 8, v1
	v_lshlrev_b32_e32 v209, 2, v130
	s_waitcnt vmcnt(37)
	v_mov_b32_e32 v158, v150
	s_waitcnt vmcnt(36)
	v_mov_b32_e32 v159, v154
	v_mov_b32_e32 v154, v151
	v_mov_b32_e32 v150, v98
	v_mov_b32_e32 v151, v132
	v_mov_b32_e32 v161, v148
	v_mov_b32_e32 v163, v156
	v_mov_b32_e32 v148, v137
	v_mov_b32_e32 v156, v153
	v_mov_b32_e32 v162, v152
	v_mov_b32_e32 v132, v99
	v_pk_add_f32 v[98:99], v[104:105], v[106:107]
	v_pk_add_f32 v[100:101], v[112:113], v[158:159]
	v_pk_add_f32 v[104:105], v[146:147], v[154:155]
	v_pk_add_f32 v[106:107], v[134:135], v[150:151]
	v_pk_add_f32 v[112:113], v[148:149], v[156:157]
	v_pk_add_f32 v[110:111], v[110:111], v[132:133]
	v_lshrrev_b32_e32 v132, 1, v0
	v_and_b32_e32 v132, 8, v132
	s_mov_b32 s0, s11
	v_pk_add_f32 v[108:109], v[160:161], v[162:163]
	s_cmpk_gt_u32 s35, 0xff
	v_pk_mul_f32 v[100:101], v[100:101], s[10:11]
	v_pk_mul_f32 v[98:99], v[98:99], s[0:1] op_sel_hi:[1,0]
	v_pk_mul_f32 v[104:105], v[104:105], s[10:11]
	v_pk_mul_f32 v[102:103], v[102:103], s[0:1] op_sel_hi:[1,0]
	v_pk_mul_f32 v[108:109], v[108:109], s[10:11]
	v_pk_mul_f32 v[106:107], v[106:107], s[0:1] op_sel_hi:[1,0]
	v_pk_mul_f32 v[112:113], v[112:113], s[10:11]
	v_pk_mul_f32 v[110:111], v[110:111], s[0:1] op_sel_hi:[1,0]
	s_mov_b32 s16, s4
	s_mov_b32 s13, 3
	s_cselect_b64 s[4:5], -1, 0
	v_mov_b32_e32 v146, v187
	s_waitcnt vmcnt(11)
	v_cvt_pk_f16_f32 v130, v166, v167
	s_waitcnt vmcnt(10)
	v_cvt_pk_f16_f32 v131, v168, v169
	ds_write2st64_b32 v1, v130, v131 offset1:8
	v_mov_b32_e32 v130, v187
	v_mov_b32_e32 v131, v187
	ds_write_b64 v188, v[130:131] offset:12288
	s_waitcnt lgkmcnt(0)
	s_barrier
	ds_read_b128 v[150:153], v186
	ds_read_b128 v[154:157], v186 offset:1024
	v_bfe_u32 v130, v0, 5, 1
	v_lshl_or_b32 v207, s28, 1, v130
	v_lshlrev_b32_e32 v130, 8, v207
	v_lshlrev_b32_e32 v131, 4, v205
	v_or3_b32 v206, v130, v131, v132
	v_mov_b32_e32 v147, v187
	v_mov_b32_e32 v148, v187
	v_mov_b32_e32 v149, v187
	s_mov_b32 s28, 0x900000
	s_mov_b32 s12, 0x4038aa3b
	s_waitcnt vmcnt(5) lgkmcnt(0)
	v_mov_b64_e32 v[130:131], v[138:139]
	s_waitcnt vmcnt(4)
	v_mov_b64_e32 v[134:135], v[142:143]
	v_mov_b64_e32 v[132:133], v[140:141]
	v_mov_b64_e32 v[136:137], v[144:145]
	s_mov_b32 s40, 0
	s_mov_b32 s41, 0xbeb17218
	s_mov_b32 s42, 0x42a00000
	s_mov_b32 s44, 0
	s_mov_b32 s45, 0x500000
	s_mov_b32 s46, 0x8000
	s_cmp_gt_u32 s35, 0xff
	s_cselect_b32 s47, 0x800, 0
	v_add_u32_e32 v252, 0x2000, v186
	v_subrev_u32_e32 v253, s47, v252
	v_add_u32_e32 v252, s47, v252
	v_add_u32_e32 v248, 0x1000, v252
	v_add_u32_e32 v249, 0x1000, v253
	s_mov_b32 s64, s6
	s_and_b32 s65, s7, 0xffff
	s_movk_i32 s66, 0xc8
	s_mov_b32 s67, 0x20000
	v_and_b32_e32 v254, 31, v0
	v_lshlrev_b32_e32 v254, 2, v254
	buffer_load_dword v255, v254, s[64:67], 0 offen offset:128
	buffer_load_dword v254, v254, s[64:67], 0 offen
	s_cmp_gt_u32 s35, 0xff
	s_cbranch_scc0 .Lmy_noperm_in
	v_swap_b32 v54, v62
	v_swap_b32 v55, v63
	v_swap_b32 v56, v64
	v_swap_b32 v57, v65
	v_swap_b32 v58, v50
	v_swap_b32 v59, v51
	v_swap_b32 v60, v52
	v_swap_b32 v61, v53
	v_swap_b32 v34, v42
	v_swap_b32 v35, v43
	v_swap_b32 v36, v44
	v_swap_b32 v37, v45
	v_swap_b32 v38, v46
	v_swap_b32 v39, v47
	v_swap_b32 v40, v48
	v_swap_b32 v41, v49
	v_swap_b32 v18, v10
	v_swap_b32 v19, v11
	v_swap_b32 v20, v12
	v_swap_b32 v21, v13
	v_swap_b32 v14, v26
	v_swap_b32 v15, v27
	v_swap_b32 v16, v28
	v_swap_b32 v17, v29
	v_swap_b32 v2, v22
	v_swap_b32 v3, v23
	v_swap_b32 v4, v24
	v_swap_b32 v5, v25
	v_swap_b32 v6, v30
	v_swap_b32 v7, v31
	v_swap_b32 v8, v32
	v_swap_b32 v9, v33
